# P13 down-GEMM units remapped so each XCD serves 2 column tiles x 16 blocks (was 1 x 32): less L2/fabric refetch of the activation tiles
# speedup vs baseline: 1.0227x; 1.0092x over previous
;     __device__ __forceinline__ bool next(int i, Unit& u) const { const int L = i * G + c; if (L >= NB * nN) return false; u.z = L / nN; u.pn = L % nN; u.pm = i; return true; }
; template <class Epi, class Sched, bool ALIGN_EPI = false, bool SP2 = false>
; __device__ __forceinline__ void gemm_phase(PG8_LAS unsigned char* lds, const Geo geo, const Sched& S, const Epi& E, const int wave_) {
;     ...
;     const int tid = tid_, wid = __builtin_amdgcn_readfirstlane(tid >> 6), lane = tid & 63, wr = wid >> 2, wc = wid & 3, fr = lane & 15, fq = lane >> 4;
;     const int nt = geo.nt;
;     unsigned voffA[2], voffB[2];
; #pragma unroll
;     for (int i = 0; i < 2; ++i) { int R, C; stage_rc(tid * 16 + i * 8192, R, C); const int Rb = Epi::PERM ? ((R & ~31) + perm32(R & 31)) : R;
;         voffA[i] = (unsigned)(R * geo.lda + C * 2); voffB[i] = (unsigned)(Rb * geo.ldb + C * 2); }
;     unsigned c0[2], c1[2], n0[2], n1[2];
; #pragma unroll
;     for (int i = 0; i < 2; ++i) { c0[i] = voffA[i]; c1[i] = voffA[i]; n0[i] = voffA[i]; n1[i] = voffA[i]; }
;     const size_t kstep = (size_t)(BK * 2);
;     const size_t hstepA = (size_t)geo.hstepA, hstepB = (size_t)geo.hstepB;
;     const unsigned ldsw = (unsigned)wid * 1024u;
;     const int aoff = lds_byte(wr * 64 + fr, fq * 8), boff = lds_byte(wc * 32 + fr, fq * 8);
;     ...
;     Unit cur, nxt; int ui = 0;
;     if (!S.next(0, cur)) return;
;     f32x4 acc[2][2][4][2];
; #pragma unroll
;     for (int a = 0; a < 2; ++a)
; #pragma unroll
;         for (int b = 0; b < 2; ++b)
; #pragma unroll
;             for (int m = 0; m < 4; ++m)
; #pragma unroll
;                 for (int n = 0; n < 2; ++n) acc[a][b][m][n] = (f32x4){0.f, 0.f, 0.f, 0.f};
;     bf16x8 At[4][2], B0[2][2], B1[2][2];
;     i32x8 At8[4], B08[2], B18[2];
;     const char* cA; const char* cB; S.ptrs(cur, cA, cB);
;     S.a_ready(cur);
;     if constexpr (Sched::GATHER) {
; #pragma unroll
;         for (int i = 0; i < 2; ++i) { int R, C; stage_rc(tid * 16 + i * 8192, R, C); c0[i] = S.row_off(0, R) + (unsigned)(C * 2); c1[i] = S.row_off(0, 128 + R) + (unsigned)(C * 2); n0[i] = c0[i]; n1[i] = c1[i]; } }
;     static_assert(SP2, "only the two-super-phase loop is kept in this file");
;     PG8_STAGE(PG8_SB(0, 0), cB, voffB); PG8_STAGE(PG8_SB(0, 1), cB + hstepB, voffB); PG8_STAGE(PG8_SA(0, 0), cA, c0); PG8_STAGE(PG8_SA(0, 1), cA + hstepA, c1);
.LBB0_1605:
	s_or_b64 exec, exec, s[4:5]
	s_add_i32 s0, 0, 0x23380
	v_mov_b32_e32 v0, s0
	s_waitcnt lgkmcnt(0)
	s_barrier
	ds_read_b32 v0, v0
	v_mov_b32_e32 v1, 0
	v_mov_b32_e32 v197, 0
	v_mbcnt_lo_u32_b32 v1, -1, v1
	v_mbcnt_hi_u32_b32 v1, -1, v1
	s_waitcnt lgkmcnt(0)
	v_readfirstlane_b32 s0, v0
	v_add_u32_e32 v12, s94, v1
	s_lshl_b32 s2, s0, 3
	s_cmp_ge_i32 s92, s2
	v_readfirstlane_b32 s12, v12
	s_cbranch_scc1 .LBB0_1627
	v_lshlrev_b32_e32 v0, 4, v12
	v_add_u32_e32 v1, 0x2000, v0
	v_ashrrev_i32_e32 v2, 31, v1
	v_lshrrev_b32_e32 v2, 22, v2
	v_add_u32_e32 v2, v1, v2
	v_ashrrev_i32_e32 v8, 10, v2
	v_bfe_i32 v5, v12, 27, 1
	v_mul_i32_i24_e32 v3, 0x400, v8
	v_lshrrev_b32_e32 v5, 22, v5
	v_sub_u32_e32 v1, v1, v3
	v_add_u32_e32 v5, v0, v5
	v_lshrrev_b32_e32 v3, 4, v1
	v_and_b32_e32 v5, 0xfffffc00, v5
	v_bitop3_b32 v1, v3, v1, 32 bitop3:0x6c
	v_sub_u32_e32 v0, v0, v5
	v_ashrrev_i32_e32 v3, 31, v1
	v_lshrrev_b32_e32 v5, 4, v0
	v_lshrrev_b32_e32 v3, 26, v3
	v_bitop3_b32 v0, v5, v0, 32 bitop3:0x6c
	v_add_u32_e32 v3, v1, v3
	v_ashrrev_i32_e32 v5, 31, v0
	v_ashrrev_i32_e32 v9, 6, v3
	v_and_b32_e32 v3, 0xc0, v3
	v_ashrrev_i32_e32 v4, 31, v12
	v_lshrrev_b32_e32 v5, 26, v5
	v_sub_u32_e32 v1, v1, v3
	v_mov_b32_e32 v3, 1
	v_lshrrev_b32_e32 v4, 26, v4
	v_add_u32_e32 v5, v0, v5
	v_lshlrev_b32_e32 v2, 5, v8
	v_ashrrev_i16_sdwa v1, v3, sext(v1) dst_sel:DWORD dst_unused:UNUSED_PAD src0_sel:DWORD src1_sel:BYTE_0
	v_add_u32_e32 v4, v12, v4
	v_ashrrev_i32_e32 v13, 6, v5
	v_and_b32_e32 v5, 0xc0, v5
	v_and_b32_e32 v2, 32, v2
	v_bfe_i32 v10, v1, 0, 16
	v_ashrrev_i32_e32 v11, 6, v4
	v_sub_u32_e32 v0, v0, v5
	v_add_lshl_u32 v1, v2, v10, 1
	v_lshlrev_b32_e32 v2, 3, v8
	v_lshlrev_b32_e32 v4, 5, v11
	v_ashrrev_i16_sdwa v0, v3, sext(v0) dst_sel:DWORD dst_unused:UNUSED_PAD src0_sel:DWORD src1_sel:BYTE_0
	v_and_b32_e32 v2, -16, v2
	v_and_b32_e32 v4, 32, v4
	v_bfe_i32 v14, v0, 0, 16
	v_add_u32_e32 v2, v9, v2
	v_add_lshl_u32 v0, v4, v14, 1
	v_and_b32_e32 v4, 3, v9
	s_mov_b32 s0, 0x1fffe0
	v_lshl_add_u32 v198, v2, 11, v1
	v_and_or_b32 v4, v2, s0, v4
	v_lshrrev_b32_e32 v5, 2, v2
	v_lshlrev_b32_e32 v2, 1, v2
	s_add_u32 s3, s78, 0x23dc8000
	v_lshlrev_b32_e32 v3, 3, v11
	v_and_b32_e32 v5, 4, v5
	v_and_b32_e32 v2, 24, v2
	s_addc_u32 s15, s79, 0
	v_and_b32_e32 v3, -16, v3
	v_or3_b32 v2, v4, v5, v2
	s_add_u32 s17, s78, 0x57dc8000
	v_add_u32_e32 v3, v13, v3
	v_lshl_add_u32 v202, v2, 11, v1
	v_and_b32_e32 v1, 3, v13
	s_addc_u32 s33, s79, 0
	v_and_or_b32 v1, v3, s0, v1
	s_and_b32 s26, s92, 7
	s_lshr_b32 s28, s92, 3
	s_lshr_b32 s1, s26, 2
	s_lshl_b32 s1, s1, 4
	s_and_b32 s26, s26, 3
	s_lshl_b32 s26, s26, 1
	s_and_b32 s0, s28, 1
	s_lshr_b32 s28, s28, 1
	s_add_i32 s1, s1, s28
	s_or_b32 s28, s26, s0
	s_mov_b32 s26, s1
	s_lshl_b32 s1, s26, 2
	v_lshl_add_u32 v200, v3, 11, v0
	v_lshrrev_b32_e32 v2, 2, v3
	v_lshlrev_b32_e32 v3, 1, v3
	s_add_i32 s1, s1, 0
	v_and_b32_e32 v2, 4, v2
	v_and_b32_e32 v3, 24, v3
	s_add_i32 s1, s1, 0x22c00
	v_or3_b32 v1, v1, v2, v3
	v_mov_b32_e32 v2, s1
	ds_read_b32 v2, v2
	s_ashr_i32 s10, s12, 6
	s_ashr_i32 s27, s26, 31
	s_waitcnt lgkmcnt(0)
	v_readfirstlane_b32 s0, v2
	s_ashr_i32 s1, s0, 31
	s_ashr_i32 s13, s12, 8
	s_lshl_b32 s8, s10, 10
	s_lshl_b64 s[6:7], s[26:27], 19
	s_lshl_b64 s[0:1], s[0:1], 22
	s_add_u32 s4, s17, s0
	s_addc_u32 s5, s33, s1
	s_ashr_i32 s29, s28, 31
	s_lshl_b64 s[0:1], s[28:29], 19
	s_add_u32 s4, s4, s0
	s_addc_u32 s5, s5, s1
	s_add_i32 s29, s8, 0
	s_add_i32 s38, s29, 0x10000
	s_add_i32 s39, s29, 0x12000
	v_lshl_add_u32 v196, v1, 11, v0
	s_mov_b32 m0, s38
	s_add_u32 s0, s4, 0x40000
	global_load_lds_dwordx4 v196, s[4:5]
	s_mov_b32 m0, s39
	s_addc_u32 s1, s5, 0
	s_add_i32 s40, s29, 0x14000
	s_add_i32 s41, s29, 0x16000
	global_load_lds_dwordx4 v202, s[4:5]
	s_mov_b32 m0, s40
	s_add_u32 s6, s3, s6
	global_load_lds_dwordx4 v196, s[0:1]
	s_mov_b32 m0, s41
	s_addc_u32 s7, s15, s7
	s_add_i32 s42, s29, 0x2000
	global_load_lds_dwordx4 v202, s[0:1]
	s_mov_b32 m0, s29
	s_add_u32 s0, s6, 0x40000
	global_load_lds_dwordx4 v200, s[6:7]
	s_mov_b32 m0, s42
	s_addc_u32 s1, s7, 0
	s_add_i32 s43, s29, 0x4000
	global_load_lds_dwordx4 v198, s[6:7]
	s_mov_b32 m0, s43
	s_add_i32 s44, s29, 0x6000
	global_load_lds_dwordx4 v200, s[0:1]
	s_mov_b32 m0, s44
	v_mov_b32_e32 v203, v197
	global_load_lds_dwordx4 v198, s[0:1]
	v_mov_b32_e32 v201, v197
	v_mov_b32_e32 v199, v197
	s_cmp_eq_u32 s13, 1
	v_lshl_add_u64 v[6:7], s[4:5], 0, v[196:197]
	v_lshl_add_u64 v[2:3], s[4:5], 0, v[202:203]
	s_mov_b64 s[0:1], 0x40000
	v_lshl_add_u64 v[0:1], s[6:7], 0, v[200:201]
	s_cselect_b64 s[8:9], -1, 0
	s_cmp_lg_u32 s13, 1
	v_lshl_add_u64 v[4:5], s[6:7], 0, v[198:199]
	s_cbranch_scc1 .LBB0_1608
	s_barrier

; template <class Epi, class Sched, bool ALIGN_EPI = false, bool SP2 = false>
; __device__ __forceinline__ void gemm_phase(PG8_LAS unsigned char* lds, const Geo geo, const Sched& S, const Epi& E, const int wave_) {
;     ...
;         const bool has_next = S.next(ui + 1, nxt);
;         const char* nA = cA; const char* nB = cB; if (has_next) S.ptrs(nxt, nA, nB);
;     __device__ __forceinline__ bool next(int i, Unit& u) const { const int L = i * G + c; if (L >= NB * nN) return false; u.z = L / nN; u.pn = L % nN; u.pm = i; return true; }
.LBB0_1611:
	s_add_i32 s53, s53, 1
	s_mul_i32 s0, s53, s83
	s_add_i32 s0, s0, s92
	s_cmp_lt_i32 s0, s2
	s_cselect_b64 s[22:23], -1, 0
	s_cmp_ge_i32 s0, s2
	s_cbranch_scc1 .LBB0_1613
	s_or_b32 s1, s0, 0xff
	s_cmp_lt_i32 s1, s2
	s_cbranch_scc0 .Lp13b_old
	s_and_b32 s1, s0, 7
	s_bfe_u32 s19, s0, 0x50003
	s_and_b32 s20, s1, 3
	s_lshl_b32 s20, s20, 1
	s_and_b32 s21, s19, 1
	s_or_b32 s20, s20, s21
	s_lshr_b32 s18, s0, 8
	s_lshl_b32 s18, s18, 5
	s_lshr_b32 s1, s1, 2
	s_lshl_b32 s1, s1, 4
	s_add_i32 s18, s18, s1
	s_lshr_b32 s19, s19, 1
	s_add_i32 s18, s18, s19
	s_branch .Lp13b_done
.Lp13b_old:
	s_ashr_i32 s18, s0, 3
	s_and_b32 s20, s0, 7
.Lp13b_done:
.LBB0_1613:
	v_cndmask_b32_e64 v0, 0, 1, s[22:23]
	v_cmp_ne_u32_e64 s[0:1], 1, v0
	s_andn2_b64 vcc, exec, s[22:23]
	s_mov_b64 s[22:23], s[6:7]
	s_mov_b64 s[24:25], s[4:5]
	s_cbranch_vccnz .LBB0_1615
	s_lshl_b32 s19, s18, 2
	s_add_i32 s19, s19, 0
	s_add_i32 s19, s19, 0x22c00
	v_mov_b32_e32 v0, s19
	ds_read_b32 v0, v0
	s_ashr_i32 s19, s18, 31
	s_lshl_b64 s[22:23], s[18:19], 19
	s_waitcnt lgkmcnt(0)
	v_readfirstlane_b32 s24, v0
	s_ashr_i32 s25, s24, 31
	s_add_u32 s22, s3, s22
	s_addc_u32 s23, s15, s23
	s_lshl_b64 s[24:25], s[24:25], 22
	s_add_u32 s19, s17, s24
	s_addc_u32 s27, s33, s25
	s_ashr_i32 s21, s20, 31
	s_lshl_b64 s[24:25], s[20:21], 19
	s_add_u32 s24, s19, s24
	s_addc_u32 s25, s27, s25
